# lists phase: CNT per-expert sums issue their 32 loads together instead of 16 dependent round trips
# speedup vs baseline: 1.0041x; 1.0041x over previous
.LBB0_952:
	v_lshl_or_b32 v96, v4, 6, v0
	v_lshlrev_b32_e32 v96, 2, v96
	v_sub_u32_e32 v97, s12, v4
	v_add_u32_e32 v97, 7, v97
	v_ashrrev_i32_e32 v97, 3, v97
	v_max_i32_e32 v97, 0, v97
	global_load_dword v64, v96, s[8:9]
	global_load_dword v65, v96, s[8:9] offset:2048
	v_add_u32_e32 v96, 0x1000, v96
	global_load_dword v66, v96, s[8:9]
	global_load_dword v67, v96, s[8:9] offset:2048
	v_add_u32_e32 v96, 0x1000, v96
	global_load_dword v68, v96, s[8:9]
	global_load_dword v69, v96, s[8:9] offset:2048
	v_add_u32_e32 v96, 0x1000, v96
	global_load_dword v70, v96, s[8:9]
	global_load_dword v71, v96, s[8:9] offset:2048
	v_add_u32_e32 v96, 0x1000, v96
	global_load_dword v72, v96, s[8:9]
	global_load_dword v73, v96, s[8:9] offset:2048
	v_add_u32_e32 v96, 0x1000, v96
	global_load_dword v74, v96, s[8:9]
	global_load_dword v75, v96, s[8:9] offset:2048
	v_add_u32_e32 v96, 0x1000, v96
	global_load_dword v76, v96, s[8:9]
	global_load_dword v77, v96, s[8:9] offset:2048
	v_add_u32_e32 v96, 0x1000, v96
	global_load_dword v78, v96, s[8:9]
	global_load_dword v79, v96, s[8:9] offset:2048
	v_add_u32_e32 v96, 0x1000, v96
	global_load_dword v80, v96, s[8:9]
	global_load_dword v81, v96, s[8:9] offset:2048
	v_add_u32_e32 v96, 0x1000, v96
	global_load_dword v82, v96, s[8:9]
	global_load_dword v83, v96, s[8:9] offset:2048
	v_add_u32_e32 v96, 0x1000, v96
	global_load_dword v84, v96, s[8:9]
	global_load_dword v85, v96, s[8:9] offset:2048
	v_add_u32_e32 v96, 0x1000, v96
	global_load_dword v86, v96, s[8:9]
	global_load_dword v87, v96, s[8:9] offset:2048
	v_add_u32_e32 v96, 0x1000, v96
	global_load_dword v88, v96, s[8:9]
	global_load_dword v89, v96, s[8:9] offset:2048
	v_add_u32_e32 v96, 0x1000, v96
	global_load_dword v90, v96, s[8:9]
	global_load_dword v91, v96, s[8:9] offset:2048
	v_add_u32_e32 v96, 0x1000, v96
	global_load_dword v92, v96, s[8:9]
	global_load_dword v93, v96, s[8:9] offset:2048
	v_add_u32_e32 v96, 0x1000, v96
	global_load_dword v94, v96, s[8:9]
	global_load_dword v95, v96, s[8:9] offset:2048
	v_mov_b32_e32 v14, 0
	v_mov_b32_e32 v15, 0
	s_waitcnt vmcnt(31)
	v_cmp_lt_u32_e32 vcc, 0, v97
	v_add_u32_e32 v15, v15, v64
	s_nop 0
	v_cndmask_b32_e32 v98, 0, v64, vcc
	v_add_u32_e32 v14, v14, v98
	s_waitcnt vmcnt(30)
	v_cmp_lt_u32_e32 vcc, 1, v97
	v_add_u32_e32 v15, v15, v65
	s_nop 0
	v_cndmask_b32_e32 v98, 0, v65, vcc
	v_add_u32_e32 v14, v14, v98
	s_waitcnt vmcnt(29)
	v_cmp_lt_u32_e32 vcc, 2, v97
	v_add_u32_e32 v15, v15, v66
	s_nop 0
	v_cndmask_b32_e32 v98, 0, v66, vcc
	v_add_u32_e32 v14, v14, v98
	s_waitcnt vmcnt(28)
	v_cmp_lt_u32_e32 vcc, 3, v97
	v_add_u32_e32 v15, v15, v67
	s_nop 0
	v_cndmask_b32_e32 v98, 0, v67, vcc
	v_add_u32_e32 v14, v14, v98
	s_waitcnt vmcnt(27)
	v_cmp_lt_u32_e32 vcc, 4, v97
	v_add_u32_e32 v15, v15, v68
	s_nop 0
	v_cndmask_b32_e32 v98, 0, v68, vcc
	v_add_u32_e32 v14, v14, v98
	s_waitcnt vmcnt(26)
	v_cmp_lt_u32_e32 vcc, 5, v97
	v_add_u32_e32 v15, v15, v69
	s_nop 0
	v_cndmask_b32_e32 v98, 0, v69, vcc
	v_add_u32_e32 v14, v14, v98
	s_waitcnt vmcnt(25)
	v_cmp_lt_u32_e32 vcc, 6, v97
	v_add_u32_e32 v15, v15, v70
	s_nop 0
	v_cndmask_b32_e32 v98, 0, v70, vcc
	v_add_u32_e32 v14, v14, v98
	s_waitcnt vmcnt(24)
	v_cmp_lt_u32_e32 vcc, 7, v97
	v_add_u32_e32 v15, v15, v71
	s_nop 0
	v_cndmask_b32_e32 v98, 0, v71, vcc
	v_add_u32_e32 v14, v14, v98
	s_waitcnt vmcnt(23)
	v_cmp_lt_u32_e32 vcc, 8, v97
	v_add_u32_e32 v15, v15, v72
	s_nop 0
	v_cndmask_b32_e32 v98, 0, v72, vcc
	v_add_u32_e32 v14, v14, v98
	s_waitcnt vmcnt(22)
	v_cmp_lt_u32_e32 vcc, 9, v97
	v_add_u32_e32 v15, v15, v73
	s_nop 0
	v_cndmask_b32_e32 v98, 0, v73, vcc
	v_add_u32_e32 v14, v14, v98
	s_waitcnt vmcnt(21)
	v_cmp_lt_u32_e32 vcc, 10, v97
	v_add_u32_e32 v15, v15, v74
	s_nop 0
	v_cndmask_b32_e32 v98, 0, v74, vcc
	v_add_u32_e32 v14, v14, v98
	s_waitcnt vmcnt(20)
	v_cmp_lt_u32_e32 vcc, 11, v97
	v_add_u32_e32 v15, v15, v75
	s_nop 0
	v_cndmask_b32_e32 v98, 0, v75, vcc
	v_add_u32_e32 v14, v14, v98
	s_waitcnt vmcnt(19)
	v_cmp_lt_u32_e32 vcc, 12, v97
	v_add_u32_e32 v15, v15, v76
	s_nop 0
	v_cndmask_b32_e32 v98, 0, v76, vcc
	v_add_u32_e32 v14, v14, v98
	s_waitcnt vmcnt(18)
	v_cmp_lt_u32_e32 vcc, 13, v97
	v_add_u32_e32 v15, v15, v77
	s_nop 0
	v_cndmask_b32_e32 v98, 0, v77, vcc
	v_add_u32_e32 v14, v14, v98
	s_waitcnt vmcnt(17)
	v_cmp_lt_u32_e32 vcc, 14, v97
	v_add_u32_e32 v15, v15, v78
	s_nop 0
	v_cndmask_b32_e32 v98, 0, v78, vcc
	v_add_u32_e32 v14, v14, v98
	s_waitcnt vmcnt(16)
	v_cmp_lt_u32_e32 vcc, 15, v97
	v_add_u32_e32 v15, v15, v79
	s_nop 0
	v_cndmask_b32_e32 v98, 0, v79, vcc
	v_add_u32_e32 v14, v14, v98
	s_waitcnt vmcnt(15)
	v_cmp_lt_u32_e32 vcc, 16, v97
	v_add_u32_e32 v15, v15, v80
	s_nop 0
	v_cndmask_b32_e32 v98, 0, v80, vcc
	v_add_u32_e32 v14, v14, v98
	s_waitcnt vmcnt(14)
	v_cmp_lt_u32_e32 vcc, 17, v97
	v_add_u32_e32 v15, v15, v81
	s_nop 0
	v_cndmask_b32_e32 v98, 0, v81, vcc
	v_add_u32_e32 v14, v14, v98
	s_waitcnt vmcnt(13)
	v_cmp_lt_u32_e32 vcc, 18, v97
	v_add_u32_e32 v15, v15, v82
	s_nop 0
	v_cndmask_b32_e32 v98, 0, v82, vcc
	v_add_u32_e32 v14, v14, v98
	s_waitcnt vmcnt(12)
	v_cmp_lt_u32_e32 vcc, 19, v97
	v_add_u32_e32 v15, v15, v83
	s_nop 0
	v_cndmask_b32_e32 v98, 0, v83, vcc
	v_add_u32_e32 v14, v14, v98
	s_waitcnt vmcnt(11)
	v_cmp_lt_u32_e32 vcc, 20, v97
	v_add_u32_e32 v15, v15, v84
	s_nop 0
	v_cndmask_b32_e32 v98, 0, v84, vcc
	v_add_u32_e32 v14, v14, v98
	s_waitcnt vmcnt(10)
	v_cmp_lt_u32_e32 vcc, 21, v97
	v_add_u32_e32 v15, v15, v85
	s_nop 0
	v_cndmask_b32_e32 v98, 0, v85, vcc
	v_add_u32_e32 v14, v14, v98
	s_waitcnt vmcnt(9)
	v_cmp_lt_u32_e32 vcc, 22, v97
	v_add_u32_e32 v15, v15, v86
	s_nop 0
	v_cndmask_b32_e32 v98, 0, v86, vcc
	v_add_u32_e32 v14, v14, v98
	s_waitcnt vmcnt(8)
	v_cmp_lt_u32_e32 vcc, 23, v97
	v_add_u32_e32 v15, v15, v87
	s_nop 0
	v_cndmask_b32_e32 v98, 0, v87, vcc
	v_add_u32_e32 v14, v14, v98
	s_waitcnt vmcnt(7)
	v_cmp_lt_u32_e32 vcc, 24, v97
	v_add_u32_e32 v15, v15, v88
	s_nop 0
	v_cndmask_b32_e32 v98, 0, v88, vcc
	v_add_u32_e32 v14, v14, v98
	s_waitcnt vmcnt(6)
	v_cmp_lt_u32_e32 vcc, 25, v97
	v_add_u32_e32 v15, v15, v89
	s_nop 0
	v_cndmask_b32_e32 v98, 0, v89, vcc
	v_add_u32_e32 v14, v14, v98
	s_waitcnt vmcnt(5)
	v_cmp_lt_u32_e32 vcc, 26, v97
	v_add_u32_e32 v15, v15, v90
	s_nop 0
	v_cndmask_b32_e32 v98, 0, v90, vcc
	v_add_u32_e32 v14, v14, v98
	s_waitcnt vmcnt(4)
	v_cmp_lt_u32_e32 vcc, 27, v97
	v_add_u32_e32 v15, v15, v91
	s_nop 0
	v_cndmask_b32_e32 v98, 0, v91, vcc
	v_add_u32_e32 v14, v14, v98
	s_waitcnt vmcnt(3)
	v_cmp_lt_u32_e32 vcc, 28, v97
	v_add_u32_e32 v15, v15, v92
	s_nop 0
	v_cndmask_b32_e32 v98, 0, v92, vcc
	v_add_u32_e32 v14, v14, v98
	s_waitcnt vmcnt(2)
	v_cmp_lt_u32_e32 vcc, 29, v97
	v_add_u32_e32 v15, v15, v93
	s_nop 0
	v_cndmask_b32_e32 v98, 0, v93, vcc
	v_add_u32_e32 v14, v14, v98
	s_waitcnt vmcnt(1)
	v_cmp_lt_u32_e32 vcc, 30, v97
	v_add_u32_e32 v15, v15, v94
	s_nop 0
	v_cndmask_b32_e32 v98, 0, v94, vcc
	v_add_u32_e32 v14, v14, v98
	s_waitcnt vmcnt(0)
	v_cmp_lt_u32_e32 vcc, 31, v97
	v_add_u32_e32 v15, v15, v95
	s_nop 0
	v_cndmask_b32_e32 v98, 0, v95, vcc
	v_add_u32_e32 v14, v14, v98
	ds_write_b32 v18, v15
	ds_write_b32 v20, v14 offset:2048
	s_waitcnt vmcnt(0) lgkmcnt(0)
	s_barrier
	s_and_saveexec_b64 s[64:65], s[54:55]
	s_cbranch_execz .LBB0_965
	ds_read2st64_b32 v[12:13], v19 offset1:1
	ds_read2st64_b32 v[14:15], v19 offset0:8 offset1:9
	s_waitcnt lgkmcnt(1)
	v_add_u32_e32 v16, v13, v12
	s_waitcnt lgkmcnt(0)
	v_add_u32_e32 v17, v15, v14
	ds_read2st64_b32 v[12:13], v19 offset0:2 offset1:3
	ds_read2st64_b32 v[14:15], v19 offset0:10 offset1:11
	s_waitcnt lgkmcnt(1)
	v_add3_u32 v16, v16, v12, v13
	s_waitcnt lgkmcnt(0)
	v_add3_u32 v17, v17, v14, v15
	ds_read2st64_b32 v[12:13], v19 offset0:4 offset1:5
	ds_read2st64_b32 v[14:15], v19 offset0:12 offset1:13
	s_waitcnt lgkmcnt(1)
	v_add3_u32 v16, v16, v12, v13
	s_waitcnt lgkmcnt(0)
	v_add3_u32 v17, v17, v14, v15
	ds_read2st64_b32 v[12:13], v19 offset0:6 offset1:7
	ds_read2st64_b32 v[14:15], v19 offset0:14 offset1:15
	s_waitcnt lgkmcnt(1)
	v_add3_u32 v13, v16, v12, v13
	s_waitcnt lgkmcnt(0)
	v_add3_u32 v12, v17, v14, v15
	ds_write_b32 v19, v12 offset:4864
	v_add_u32_e32 v12, 0xff, v13
	v_and_b32_e32 v14, 0xffffff00, v12
	ds_bpermute_b32 v12, v21, v14
	s_waitcnt lgkmcnt(0)
	v_cndmask_b32_e64 v12, 0, v12, s[40:41]
	v_add_u32_e32 v12, v12, v14
	ds_bpermute_b32 v15, v22, v12
	s_waitcnt lgkmcnt(0)
	v_cndmask_b32_e64 v15, v15, 0, s[42:43]
	v_add_u32_e32 v12, v15, v12
	ds_bpermute_b32 v15, v23, v12
	s_waitcnt lgkmcnt(0)
	v_cndmask_b32_e64 v15, v15, 0, s[44:45]
	v_add_u32_e32 v12, v15, v12
	ds_bpermute_b32 v15, v24, v12
	s_waitcnt lgkmcnt(0)
	v_cndmask_b32_e64 v15, v15, 0, s[46:47]
	v_add_u32_e32 v12, v15, v12
	ds_bpermute_b32 v15, v25, v12
	s_waitcnt lgkmcnt(0)
	v_cndmask_b32_e64 v15, v15, 0, s[48:49]
	v_add_u32_e32 v12, v15, v12
	ds_bpermute_b32 v15, v26, v12
	s_waitcnt lgkmcnt(0)
	v_cndmask_b32_e64 v15, v15, 0, s[50:51]
	v_add_u32_e32 v12, v15, v12
	v_sub_u32_e32 v14, v12, v14
	ds_write2st64_b32 v19, v13, v14 offset0:16 offset1:17
	s_and_b64 exec, exec, s[52:53]
	ds_write_b32 v1, v12 offset:4608
